# stack: NORM_A/B/C next-row loads in flight + FoX counted vmcnt at K/V staging + GEMM barrier handoff trims (setprio moved across barriers, redundant lgkmcnt removed) m1
# speedup vs baseline: 1.0415x; 1.0415x over previous
.LBB0_1870:
	s_add_i32 s0, s12, -1
	v_mov_b32_e32 v214, v203
	v_add_u32_e32 v94, 0x11100, v213
	ds_read_b128 v[82:85], v214 offset:16384
	ds_read_b128 v[66:69], v94
	ds_read_b128 v[70:73], v94 offset:32
	ds_read_b128 v[74:77], v94 offset:64
	ds_read_b128 v[78:81], v94 offset:96
	ds_read_b128 v[178:181], v214 offset:24576
	v_xor_b32_e32 v182, 32, v214
	v_xor_b32_e32 v186, 64, v214
	s_waitcnt lgkmcnt(1)
	v_mfma_f32_32x32x16_bf16 v[66:81], v[82:85], v[158:161], v[66:81]
	ds_read_b128 v[82:85], v94 offset:128
	ds_read_b128 v[86:89], v94 offset:160
	ds_read_b128 v[90:93], v94 offset:192
	ds_read_b128 v[94:97], v94 offset:224
	v_xor_b32_e32 v220, 0x60, v214
	v_xor_b32_e32 v228, 0x80, v214
	v_xor_b32_e32 v232, 0xa0, v214
	v_xor_b32_e32 v240, 0xc0, v214
	v_xor_b32_e32 v214, 0xe0, v214
	v_exp_f32_e32 v248, v115
	s_waitcnt lgkmcnt(0)
	v_mfma_f32_32x32x16_bf16 v[82:97], v[178:181], v[158:161], v[82:97]
	ds_read_b128 v[178:181], v182 offset:16384
	ds_read_b128 v[182:185], v182 offset:24576
	v_exp_f32_e32 v249, v116
	v_exp_f32_e32 v250, v117
	v_exp_f32_e32 v118, v118
	v_exp_f32_e32 v119, v119
	v_exp_f32_e32 v120, v120
	s_waitcnt lgkmcnt(1)
	v_mfma_f32_32x32x16_bf16 v[66:81], v[178:181], v[154:157], v[66:81]
	ds_read_b128 v[178:181], v186 offset:16384
	ds_read_b128 v[186:189], v186 offset:24576
	ds_read_b128 v[190:193], v220 offset:16384
	ds_read_b128 v[220:223], v220 offset:24576
	ds_read_b128 v[224:227], v228 offset:16384
	ds_read_b128 v[228:231], v228 offset:24576
	v_exp_f32_e32 v121, v121
	v_exp_f32_e32 v122, v122
	v_exp_f32_e32 v123, v123
	v_exp_f32_e32 v124, v124
	s_waitcnt lgkmcnt(6)
	v_mfma_f32_32x32x16_bf16 v[82:97], v[182:185], v[154:157], v[82:97]
	ds_read_b128 v[182:185], v232 offset:16384
	ds_read_b128 v[232:235], v232 offset:24576
	ds_read_b128 v[236:239], v240 offset:16384
	ds_read_b128 v[240:243], v240 offset:24576
	v_exp_f32_e32 v125, v125
	v_exp_f32_e32 v126, v126
	v_exp_f32_e32 v127, v127
	v_exp_f32_e32 v128, v128
	v_exp_f32_e32 v129, v129
	s_waitcnt lgkmcnt(9)
	v_mfma_f32_32x32x16_bf16 v[66:81], v[178:181], v[150:153], v[66:81]
	ds_read_b128 v[178:181], v214 offset:16384
	ds_read_b128 v[244:247], v214 offset:24576
	v_exp_f32_e32 v214, v114
	v_add_f32_e32 v114, 0, v98
	v_add_f32_e32 v114, v99, v114
	v_add_f32_e32 v114, v100, v114
	v_add_f32_e32 v114, v101, v114
	v_add_f32_e32 v114, v102, v114
	s_waitcnt lgkmcnt(10)
	v_mfma_f32_32x32x16_bf16 v[82:97], v[186:189], v[150:153], v[82:97]
	v_add_f32_e32 v114, v103, v114
	v_add_f32_e32 v114, v104, v114
	v_add_f32_e32 v114, v105, v114
	v_add_f32_e32 v114, v106, v114
	v_add_f32_e32 v114, v107, v114
	v_add_f32_e32 v114, v108, v114
	v_add_f32_e32 v114, v109, v114
	s_waitcnt lgkmcnt(9)
	v_mfma_f32_32x32x16_bf16 v[66:81], v[190:193], v[146:149], v[66:81]
	v_add_f32_e32 v114, v110, v114
	v_add_f32_e32 v114, v111, v114
	v_add_f32_e32 v114, v112, v114
	v_add_f32_e32 v114, v113, v114
	v_add_f32_e32 v114, v214, v114
	v_add_f32_e32 v114, v248, v114
	v_add_f32_e32 v114, v249, v114
	s_waitcnt lgkmcnt(8)
	v_mfma_f32_32x32x16_bf16 v[82:97], v[220:223], v[146:149], v[82:97]
	v_add_f32_e32 v114, v250, v114
	v_add_f32_e32 v114, v118, v114
	v_add_f32_e32 v114, v119, v114
	v_add_f32_e32 v114, v120, v114
	v_add_f32_e32 v114, v121, v114
	v_add_f32_e32 v114, v122, v114
	v_add_f32_e32 v114, v123, v114
	s_waitcnt lgkmcnt(7)
	v_mfma_f32_32x32x16_bf16 v[66:81], v[224:227], v[142:145], v[66:81]
	v_add_f32_e32 v114, v124, v114
	v_add_f32_e32 v114, v125, v114
	v_add_f32_e32 v114, v126, v114
	v_add_f32_e32 v114, v127, v114
	v_add_f32_e32 v114, v128, v114
	v_add_f32_e32 v220, v129, v114
	v_mov_b32_e32 v221, v220
	s_waitcnt lgkmcnt(6)
	v_mfma_f32_32x32x16_bf16 v[82:97], v[228:231], v[142:145], v[82:97]
	v_cvt_pk_bf16_f32 v114, v98, v99
	v_cvt_pk_bf16_f32 v115, v100, v101
	v_cvt_pk_bf16_f32 v116, v102, v103
	v_cvt_pk_bf16_f32 v117, v104, v105
	v_cvt_pk_bf16_f32 v106, v106, v107
	v_cvt_pk_bf16_f32 v107, v108, v109
	v_cvt_pk_bf16_f32 v108, v110, v111
	s_waitcnt lgkmcnt(5)
	v_mfma_f32_32x32x16_bf16 v[66:81], v[182:185], v[138:141], v[66:81]
	v_cvt_pk_bf16_f32 v109, v112, v113
	v_cvt_pk_bf16_f32 v102, v214, v248
	v_cvt_pk_bf16_f32 v103, v249, v250
	v_cvt_pk_bf16_f32 v104, v118, v119
	v_cvt_pk_bf16_f32 v105, v120, v121
	v_cvt_pk_bf16_f32 v98, v122, v123
	v_cvt_pk_bf16_f32 v99, v124, v125
	s_waitcnt lgkmcnt(4)
	v_mfma_f32_32x32x16_bf16 v[82:97], v[232:235], v[138:141], v[82:97]
	v_cvt_pk_bf16_f32 v100, v126, v127
	v_cvt_pk_bf16_f32 v101, v128, v129
	v_permlane32_swap_b32_e32 v220, v221
	v_permlane32_swap_b32_e32 v114, v116
	v_permlane32_swap_b32_e32 v115, v117
	s_waitcnt lgkmcnt(3)
	v_mfma_f32_32x32x16_bf16 v[66:81], v[236:239], v[134:137], v[66:81]
	v_permlane32_swap_b32_e32 v106, v108
	v_permlane32_swap_b32_e32 v107, v109
	v_permlane32_swap_b32_e32 v102, v104
	v_permlane32_swap_b32_e32 v103, v105
	s_waitcnt lgkmcnt(2)
	v_mfma_f32_32x32x16_bf16 v[82:97], v[240:243], v[134:137], v[82:97]
	v_permlane32_swap_b32_e32 v98, v100
	v_permlane32_swap_b32_e32 v99, v101
	s_waitcnt lgkmcnt(1)
	v_mfma_f32_32x32x16_bf16 v[66:81], v[178:181], v[130:133], v[66:81]
	s_waitcnt lgkmcnt(0)
	v_mfma_f32_32x32x16_bf16 v[82:97], v[244:247], v[130:133], v[82:97]
	s_add_i32 s0, s38, 0x40000
	s_ashr_i32 s1, s0, 31
	s_lshl_b64 s[0:1], s[0:1], 1
	s_add_u32 s0, s36, s0
	s_addc_u32 s1, s37, s1
	v_lshl_add_u64 v[110:111], s[0:1], 0, v[194:195]
	s_waitcnt vmcnt(3)
	ds_write_b128 v206, v[162:165] offset:16384
	s_waitcnt vmcnt(2)
	ds_write_b128 v206, v[166:169] offset:24576
	v_add_co_u32_e32 v110, vcc, 0x20000, v110
	s_nop 1
	v_addc_co_u32_e32 v111, vcc, 0, v111, vcc
	global_load_dwordx4 v[162:165], v194, s[0:1]
	global_load_dwordx4 v[166:169], v[110:111], off
	s_add_i32 s39, s58, 1
	s_add_i32 s0, s58, 64
	s_cmp_le_i32 s0, s43
	s_cselect_b64 s[0:1], -1, 0
	s_cmp_gt_i32 s39, s57
	s_cselect_b64 s[40:41], -1, 0
	s_and_b64 s[0:1], s[0:1], s[40:41]
	s_and_b64 vcc, exec, s[0:1]
	s_cbranch_vccnz .LBB0_1872
	v_subrev_u32_e32 v110, 64, v219
	v_cmp_gt_u32_e32 vcc, s50, v110
	v_add_u32_e32 v110, 0xffffffa0, v219
	s_nop 0
	v_cndmask_b32_e32 v66, v207, v66, vcc
	v_cmp_gt_u32_e32 vcc, s50, v110
	v_add_u32_e32 v110, 0xffffffbf, v219
	s_nop 0
	v_cndmask_b32_e32 v82, v207, v82, vcc
	v_cmp_gt_u32_e32 vcc, s50, v110
	v_add_u32_e32 v110, 0xffffff9f, v219
	s_nop 0
	v_cndmask_b32_e32 v67, v207, v67, vcc
	v_cmp_gt_u32_e32 vcc, s50, v110
	v_add_u32_e32 v110, 0xffffffbe, v219
	s_nop 0
	v_cndmask_b32_e32 v83, v207, v83, vcc
	v_cmp_gt_u32_e32 vcc, s50, v110
	v_add_u32_e32 v110, 0xffffff9e, v219
	s_nop 0
	v_cndmask_b32_e32 v68, v207, v68, vcc
	v_cmp_gt_u32_e32 vcc, s50, v110
	v_add_u32_e32 v110, 0xffffffbd, v219
	s_nop 0
	v_cndmask_b32_e32 v84, v207, v84, vcc
	v_cmp_gt_u32_e32 vcc, s50, v110
	v_add_u32_e32 v110, 0xffffff9d, v219
	s_nop 0
	v_cndmask_b32_e32 v69, v207, v69, vcc
	v_cmp_gt_u32_e32 vcc, s50, v110
	v_add_u32_e32 v110, 0xffffffb8, v219
	s_nop 0
	v_cndmask_b32_e32 v85, v207, v85, vcc
	v_cmp_gt_u32_e32 vcc, s50, v110
	v_add_u32_e32 v110, 0xffffff98, v219
	s_nop 0
	v_cndmask_b32_e32 v70, v207, v70, vcc
	v_cmp_gt_u32_e32 vcc, s50, v110
	v_add_u32_e32 v110, 0xffffffb7, v219
	s_nop 0
	v_cndmask_b32_e32 v86, v207, v86, vcc
	v_cmp_gt_u32_e32 vcc, s50, v110
	v_add_u32_e32 v110, 0xffffff97, v219
	s_nop 0
	v_cndmask_b32_e32 v71, v207, v71, vcc
	v_cmp_gt_u32_e32 vcc, s50, v110
	v_add_u32_e32 v110, 0xffffffb6, v219
	s_nop 0
	v_cndmask_b32_e32 v87, v207, v87, vcc
	v_cmp_gt_u32_e32 vcc, s50, v110
	v_add_u32_e32 v110, 0xffffff96, v219
	s_nop 0
	v_cndmask_b32_e32 v72, v207, v72, vcc
	v_cmp_gt_u32_e32 vcc, s50, v110
	v_add_u32_e32 v110, 0xffffffb5, v219
	s_nop 0
	v_cndmask_b32_e32 v88, v207, v88, vcc
	v_cmp_gt_u32_e32 vcc, s50, v110
	v_add_u32_e32 v110, 0xffffff95, v219
	s_nop 0
	v_cndmask_b32_e32 v73, v207, v73, vcc
	v_cmp_gt_u32_e32 vcc, s50, v110
	v_add_u32_e32 v110, 0xffffffb0, v219
	s_nop 0
	v_cndmask_b32_e32 v89, v207, v89, vcc
	v_cmp_gt_u32_e32 vcc, s50, v110
	v_add_u32_e32 v110, 0xffffff90, v219
	s_nop 0
	v_cndmask_b32_e32 v74, v207, v74, vcc
	v_cmp_gt_u32_e32 vcc, s50, v110
	v_add_u32_e32 v110, 0xffffffaf, v219
	s_nop 0
	v_cndmask_b32_e32 v90, v207, v90, vcc
	v_cmp_gt_u32_e32 vcc, s50, v110
	v_add_u32_e32 v110, 0xffffff8f, v219
	s_nop 0
	v_cndmask_b32_e32 v75, v207, v75, vcc
	v_cmp_gt_u32_e32 vcc, s50, v110
	v_add_u32_e32 v110, 0xffffffae, v219
	s_nop 0
	v_cndmask_b32_e32 v91, v207, v91, vcc
	v_cmp_gt_u32_e32 vcc, s50, v110
	v_add_u32_e32 v110, 0xffffff8e, v219
	s_nop 0
	v_cndmask_b32_e32 v76, v207, v76, vcc
	v_cmp_gt_u32_e32 vcc, s50, v110
	v_add_u32_e32 v110, 0xffffffad, v219
	s_nop 0
	v_cndmask_b32_e32 v92, v207, v92, vcc
	v_cmp_gt_u32_e32 vcc, s50, v110
	v_add_u32_e32 v110, 0xffffff8d, v219
	s_nop 0
	v_cndmask_b32_e32 v77, v207, v77, vcc
	v_cmp_gt_u32_e32 vcc, s50, v110
	v_add_u32_e32 v110, 0xffffffa8, v219
	s_nop 0
	v_cndmask_b32_e32 v93, v207, v93, vcc
	v_cmp_gt_u32_e32 vcc, s50, v110
	v_add_u32_e32 v110, 0xffffff88, v219
	s_nop 0
	v_cndmask_b32_e32 v78, v207, v78, vcc
	v_cmp_gt_u32_e32 vcc, s50, v110
	v_add_u32_e32 v110, 0xffffffa7, v219
	s_nop 0
	v_cndmask_b32_e32 v94, v207, v94, vcc
	v_cmp_gt_u32_e32 vcc, s50, v110
	v_add_u32_e32 v110, 0xffffff87, v219
	s_nop 0
	v_cndmask_b32_e32 v79, v207, v79, vcc
	v_cmp_gt_u32_e32 vcc, s50, v110
	v_add_u32_e32 v110, 0xffffffa6, v219
	s_nop 0
	v_cndmask_b32_e32 v95, v207, v95, vcc
	v_cmp_gt_u32_e32 vcc, s50, v110
	v_add_u32_e32 v110, 0xffffff86, v219
	s_nop 0
	v_cndmask_b32_e32 v80, v207, v80, vcc
	v_cmp_gt_u32_e32 vcc, s50, v110
	v_add_u32_e32 v110, 0xffffffa5, v219
	s_nop 0
	v_cndmask_b32_e32 v96, v207, v96, vcc
	v_cmp_gt_u32_e32 vcc, s50, v110
	v_add_u32_e32 v110, 0xffffff85, v219
	s_nop 0
	v_cndmask_b32_e32 v81, v207, v81, vcc
	v_cmp_gt_u32_e32 vcc, s50, v110
	s_nop 1
	v_cndmask_b32_e32 v97, v207, v97, vcc
.LBB0_1872:
	ds_read_b64_tr_b16 v[110:111], v201 offset:0
	ds_read_b64_tr_b16 v[112:113], v201 offset:0x800
	ds_read_b64_tr_b16 v[118:119], v201 offset:0x1000
	ds_read_b64_tr_b16 v[120:121], v201 offset:0x1800
	ds_read_b64_tr_b16 v[122:123], v201 offset:0x2000
	ds_read_b64_tr_b16 v[124:125], v201 offset:0x2800
	ds_read_b64_tr_b16 v[126:127], v201 offset:0x3000
	ds_read_b64_tr_b16 v[128:129], v201 offset:0x3800
	s_waitcnt lgkmcnt(0)
	s_nop 0
	v_mfma_f32_32x32x16_bf16 v[50:65], v[114:117], v[110:113], v[50:65]
	v_max_f32_e32 v190, v67, v67
	v_max_f32_e32 v191, v66, v66
	v_max_f32_e32 v190, v191, v190
	v_max3_f32 v190, v190, v68, v69
	v_max3_f32 v190, v190, v70, v71
	ds_read_b64_tr_b16 v[178:179], v201 offset:0x200
	ds_read_b64_tr_b16 v[180:181], v201 offset:0xa00
	v_mfma_f32_32x32x16_bf16 v[50:65], v[106:109], v[118:121], v[50:65]
	v_max3_f32 v118, v190, v72, v73
	v_max3_f32 v118, v118, v74, v75
	v_max3_f32 v118, v118, v76, v77
	v_max3_f32 v118, v118, v78, v79
	v_max3_f32 v118, v118, v80, v81
	v_max3_f32 v118, v118, v82, v83
	v_max3_f32 v118, v118, v84, v85
	v_mfma_f32_32x32x16_bf16 v[50:65], v[102:105], v[122:125], v[50:65]
	ds_read_b64_tr_b16 v[182:183], v201 offset:0x1200
	v_max3_f32 v118, v118, v86, v87
	ds_read_b64_tr_b16 v[184:185], v201 offset:0x1a00
	v_max3_f32 v118, v118, v88, v89
	ds_read_b64_tr_b16 v[186:187], v201 offset:0x2200
	v_max3_f32 v118, v118, v90, v91
	ds_read_b64_tr_b16 v[188:189], v201 offset:0x2a00
	v_mfma_f32_32x32x16_bf16 v[50:65], v[98:101], v[126:129], v[50:65]
	v_max3_f32 v118, v118, v92, v93
	ds_read_b64_tr_b16 v[110:111], v201 offset:0x3200
	v_max3_f32 v118, v118, v94, v95
	ds_read_b64_tr_b16 v[112:113], v201 offset:0x3a00
	v_max3_f32 v118, v118, v96, v97
	v_mov_b32_e32 v119, v118
	s_waitcnt lgkmcnt(0)
	s_nop 1
	v_permlane32_swap_b32_e32 v118, v119
	v_max_f32_e32 v119, v119, v119
	v_max_f32_e32 v118, v118, v118
	v_max_f32_e32 v190, v118, v119
	v_mfma_f32_32x32x16_bf16 v[34:49], v[114:117], v[178:181], v[34:49]
	v_sub_f32_e32 v191, v190, v215
	ds_read_b64_tr_b16 v[118:119], v201 offset:0x400
	v_mul_f32_e32 v191, 0x3db504f3, v191
	ds_read_b64_tr_b16 v[120:121], v201 offset:0xc00
	v_cmp_ge_f32_e32 vcc, s51, v191
	ds_read_b64_tr_b16 v[122:123], v201 offset:0x1400
	s_cmp_eq_u64 vcc, exec
	v_mfma_f32_32x32x16_bf16 v[34:49], v[106:109], v[182:185], v[34:49]
	v_max_f32_e32 v191, v215, v215
	ds_read_b64_tr_b16 v[124:125], v201 offset:0x1c00
	v_max_f32_e32 v182, v191, v190
	s_cselect_b64 vcc, -1, 0
	ds_read_b64_tr_b16 v[126:127], v201 offset:0x2400
	v_cndmask_b32_e32 v223, v182, v215, vcc
	ds_read_b64_tr_b16 v[128:129], v201 offset:0x2c00
	v_mfma_f32_32x32x16_bf16 v[34:49], v[102:105], v[186:189], v[34:49]
	v_mul_f32_e32 v182, 0xbe0293ee, v223
	ds_read_b64_tr_b16 v[178:179], v201 offset:0x3400
	v_fma_f32 v80, v80, s14, v182
	v_fma_f32 v81, v81, s14, v182
	v_fma_f32 v78, v78, s14, v182
	v_fma_f32 v79, v79, s14, v182
	v_pk_fma_f32 v[76:77], v[76:77], s[14:15], v[182:183] op_sel_hi:[1,0,0]
	v_pk_fma_f32 v[74:75], v[74:75], s[14:15], v[182:183] op_sel_hi:[1,0,0]
	v_pk_fma_f32 v[72:73], v[72:73], s[14:15], v[182:183] op_sel_hi:[1,0,0]
	v_mfma_f32_32x32x16_bf16 v[34:49], v[98:101], v[110:113], v[34:49]
	v_fma_f32 v70, v70, s14, v182
	v_fma_f32 v71, v71, s14, v182
	v_fma_f32 v68, v68, s14, v182
	v_fma_f32 v69, v69, s14, v182
	v_fma_f32 v66, v66, s14, v182
	v_fma_f32 v67, v67, s14, v182
	v_pk_fma_f32 v[96:97], v[96:97], s[14:15], v[182:183] op_sel_hi:[1,0,0]
	v_pk_fma_f32 v[94:95], v[94:95], s[14:15], v[182:183] op_sel_hi:[1,0,0]
	v_pk_fma_f32 v[92:93], v[92:93], s[14:15], v[182:183] op_sel_hi:[1,0,0]
	v_pk_fma_f32 v[90:91], v[90:91], s[14:15], v[182:183] op_sel_hi:[1,0,0]
	v_pk_fma_f32 v[88:89], v[88:89], s[14:15], v[182:183] op_sel_hi:[1,0,0]
	v_pk_fma_f32 v[86:87], v[86:87], s[14:15], v[182:183] op_sel_hi:[1,0,0]
	v_pk_fma_f32 v[84:85], v[84:85], s[14:15], v[182:183] op_sel_hi:[1,0,0]
	v_pk_fma_f32 v[82:83], v[82:83], s[14:15], v[182:183] op_sel_hi:[1,0,0]
	ds_read_b64_tr_b16 v[180:181], v201 offset:0x3c00
	s_nop 0
	s_waitcnt lgkmcnt(0)
	v_mfma_f32_32x32x16_bf16 v[18:33], v[114:117], v[118:121], v[18:33]
	ds_read_b64_tr_b16 v[110:111], v201 offset:0x600
	ds_read_b64_tr_b16 v[112:113], v201 offset:0xe00
	ds_read_b64_tr_b16 v[118:119], v201 offset:0x1600
	ds_read_b64_tr_b16 v[120:121], v201 offset:0x1e00
	v_exp_f32_e32 v66, v66
	v_exp_f32_e32 v67, v67
	v_exp_f32_e32 v68, v68
	v_mfma_f32_32x32x16_bf16 v[18:33], v[106:109], v[122:125], v[18:33]
	ds_read_b64_tr_b16 v[122:123], v201 offset:0x2600
	ds_read_b64_tr_b16 v[124:125], v201 offset:0x2e00
	v_exp_f32_e32 v69, v69
	v_exp_f32_e32 v70, v70
	v_exp_f32_e32 v71, v71
	v_exp_f32_e32 v72, v72
	v_exp_f32_e32 v73, v73
	v_mfma_f32_32x32x16_bf16 v[18:33], v[102:105], v[126:129], v[18:33]
	ds_read_b64_tr_b16 v[126:127], v201 offset:0x3600
	ds_read_b64_tr_b16 v[128:129], v201 offset:0x3e00
	s_waitcnt lgkmcnt(0)
	v_mfma_f32_32x32x16_bf16 v[18:33], v[98:101], v[178:181], v[18:33]
	v_mfma_f32_32x32x16_bf16 v[2:17], v[114:117], v[110:113], v[2:17]
	v_exp_f32_e32 v74, v74
	v_exp_f32_e32 v75, v75
	v_exp_f32_e32 v76, v76
	v_exp_f32_e32 v77, v77
	v_exp_f32_e32 v78, v78
	v_exp_f32_e32 v79, v79
	v_exp_f32_e32 v80, v80
	v_mfma_f32_32x32x16_bf16 v[2:17], v[106:109], v[118:121], v[2:17]
	v_exp_f32_e32 v81, v81
	s_waitcnt vmcnt(2)
	ds_write_b128 v208, v[170:173] offset:32768
	ds_write_b128 v208, v[174:177] offset:40960
	v_mfma_f32_32x32x16_bf16 v[2:17], v[102:105], v[122:125], v[2:17]
	v_mfma_f32_32x32x16_bf16 v[2:17], v[98:101], v[126:129], v[2:17]
	s_mov_b64 s[0:1], exec
	v_readlane_b32 s40, v254, 7
	v_readlane_b32 s41, v254, 8
	s_and_b64 s[40:41], s[0:1], s[40:41]
	s_mov_b64 exec, s[40:41]
	v_add_u32_e32 v99, 0, v198
	v_xor_b32_e32 v98, 0x80000000, v197
	v_add_u32_e32 v99, 0x11000, v99
	ds_write_b32 v99, v98
	s_or_b64 exec, exec, s[0:1]
	s_add_i32 s0, s12, 1
	s_cmp_lt_i32 s0, s56
	s_cselect_b64 s[40:41], -1, 0
	s_cmp_ge_i32 s0, s56
	s_cbranch_scc1 .LBB0_1878
	s_add_i32 s0, s38, 0x20000
	s_ashr_i32 s1, s0, 31
	s_lshl_b64 s[0:1], s[0:1], 1
	s_add_u32 s0, s30, s0
	s_addc_u32 s1, s31, s1
	v_lshl_add_u64 v[98:99], s[0:1], 0, v[194:195]
	v_add_co_u32_e32 v98, vcc, 0x20000, v98
	s_nop 1
	v_addc_co_u32_e32 v99, vcc, 0, v99, vcc
	global_load_dwordx4 v[170:173], v194, s[0:1]
	global_load_dwordx4 v[174:177], v[98:99], off
	s_mov_b64 s[0:1], exec
	v_readlane_b32 s60, v254, 7
	v_readlane_b32 s61, v254, 8
	s_and_b64 s[60:61], s[0:1], s[60:61]
	s_mov_b64 exec, s[60:61]
	s_cbranch_execz .LBB0_1877
	v_add_u32_e32 v98, s58, v0
	v_add_u32_e32 v98, 0xffffff81, v98
	v_ashrrev_i32_e32 v99, 31, v98
	v_lshl_add_u64 v[98:99], v[98:99], 2, s[34:35]
	global_load_dword v197, v[98:99], off

.LBB0_1882:
	v_mov_b32_e32 v214, v203
	ds_read_b128 v[114:117], v214
	ds_read_b128 v[98:101], v218
	ds_read_b128 v[102:105], v218 offset:32
	ds_read_b128 v[106:109], v218 offset:64
	ds_read_b128 v[110:113], v218 offset:96
	ds_read_b128 v[178:181], v214 offset:8192
	v_xor_b32_e32 v182, 32, v214
	v_xor_b32_e32 v186, 64, v214
	v_xor_b32_e32 v215, 0x60, v214
	s_waitcnt lgkmcnt(1)
	v_mfma_f32_32x32x16_bf16 v[98:113], v[114:117], v[158:161], v[98:113]
	ds_read_b128 v[114:117], v218 offset:128
	ds_read_b128 v[118:121], v218 offset:160
	ds_read_b128 v[122:125], v218 offset:192
	ds_read_b128 v[126:129], v218 offset:224
	v_exp_f32_e32 v82, v82
	v_exp_f32_e32 v83, v83
	v_exp_f32_e32 v84, v84
	v_exp_f32_e32 v85, v85
	v_exp_f32_e32 v86, v86
	v_exp_f32_e32 v87, v87
	s_waitcnt lgkmcnt(0)
	v_mfma_f32_32x32x16_bf16 v[114:129], v[178:181], v[158:161], v[114:129]
	ds_read_b128 v[178:181], v182
	ds_read_b128 v[182:185], v182 offset:8192
	v_exp_f32_e32 v88, v88
	v_exp_f32_e32 v89, v89
	v_exp_f32_e32 v90, v90
	v_exp_f32_e32 v91, v91
	v_exp_f32_e32 v92, v92
	s_waitcnt lgkmcnt(1)
	v_mfma_f32_32x32x16_bf16 v[98:113], v[178:181], v[154:157], v[98:113]
	ds_read_b128 v[178:181], v186
	ds_read_b128 v[186:189], v186 offset:8192
	ds_read_b128 v[190:193], v215
	ds_read_b128 v[224:227], v215 offset:8192
	v_xor_b32_e32 v215, 0x80, v214
	ds_read_b128 v[228:231], v215
	ds_read_b128 v[232:235], v215 offset:8192
	v_xor_b32_e32 v215, 0xa0, v214
	v_exp_f32_e32 v93, v93
	v_exp_f32_e32 v94, v94
	s_waitcnt lgkmcnt(6)
	v_mfma_f32_32x32x16_bf16 v[114:129], v[182:185], v[154:157], v[114:129]
	ds_read_b128 v[182:185], v215
	ds_read_b128 v[236:239], v215 offset:8192
	v_xor_b32_e32 v215, 0xc0, v214
	ds_read_b128 v[240:243], v215
	ds_read_b128 v[244:247], v215 offset:8192
	v_xor_b32_e32 v214, 0xe0, v214
	v_exp_f32_e32 v95, v95
	v_exp_f32_e32 v96, v96
	v_exp_f32_e32 v97, v97
	s_waitcnt lgkmcnt(9)
	v_mfma_f32_32x32x16_bf16 v[98:113], v[178:181], v[150:153], v[98:113]
	ds_read_b128 v[178:181], v214
	ds_read_b128 v[248:251], v214 offset:8192
	s_waitcnt lgkmcnt(10)
	v_mfma_f32_32x32x16_bf16 v[114:129], v[186:189], v[150:153], v[114:129]
	v_add_f32_e32 v186, 0, v66
	v_add_f32_e32 v186, v67, v186
	v_add_f32_e32 v186, v68, v186
	v_add_f32_e32 v186, v69, v186
	v_add_f32_e32 v186, v70, v186
	v_add_f32_e32 v186, v71, v186
	v_add_f32_e32 v186, v72, v186
	s_waitcnt lgkmcnt(9)
	v_mfma_f32_32x32x16_bf16 v[98:113], v[190:193], v[146:149], v[98:113]
	v_add_f32_e32 v186, v73, v186
	v_add_f32_e32 v186, v74, v186
	v_add_f32_e32 v186, v75, v186
	v_add_f32_e32 v186, v76, v186
	v_add_f32_e32 v186, v77, v186
	v_add_f32_e32 v186, v78, v186
	v_add_f32_e32 v186, v79, v186
	s_waitcnt lgkmcnt(8)
	v_mfma_f32_32x32x16_bf16 v[114:129], v[224:227], v[146:149], v[114:129]
	v_add_f32_e32 v186, v80, v186
	v_add_f32_e32 v186, v81, v186
	v_add_f32_e32 v186, v82, v186
	v_add_f32_e32 v186, v83, v186
	v_add_f32_e32 v186, v84, v186
	v_add_f32_e32 v186, v85, v186
	v_add_f32_e32 v186, v86, v186
	s_waitcnt lgkmcnt(7)
	v_mfma_f32_32x32x16_bf16 v[98:113], v[228:231], v[142:145], v[98:113]
	v_add_f32_e32 v186, v87, v186
	v_add_f32_e32 v186, v88, v186
	v_add_f32_e32 v186, v89, v186
	v_add_f32_e32 v186, v90, v186
	s_waitcnt lgkmcnt(6)
	v_mfma_f32_32x32x16_bf16 v[114:129], v[232:235], v[142:145], v[114:129]
	s_waitcnt lgkmcnt(5)
	v_mfma_f32_32x32x16_bf16 v[98:113], v[182:185], v[138:141], v[98:113]
	v_add_f32_e32 v182, v91, v186
	v_add_f32_e32 v182, v92, v182
	v_add_f32_e32 v182, v93, v182
	v_add_f32_e32 v182, v94, v182
	v_add_f32_e32 v182, v95, v182
	v_add_f32_e32 v182, v96, v182
	v_add_f32_e32 v224, v97, v182
	s_waitcnt lgkmcnt(4)
	v_mfma_f32_32x32x16_bf16 v[114:129], v[236:239], v[138:141], v[114:129]
	v_mov_b32_e32 v225, v224
	v_cvt_pk_bf16_f32 v186, v66, v67
	v_cvt_pk_bf16_f32 v187, v68, v69
	v_cvt_pk_bf16_f32 v188, v70, v71
	v_cvt_pk_bf16_f32 v189, v72, v73
	v_cvt_pk_bf16_f32 v190, v74, v75
	v_cvt_pk_bf16_f32 v191, v76, v77
	s_waitcnt lgkmcnt(3)
	v_mfma_f32_32x32x16_bf16 v[98:113], v[240:243], v[134:137], v[98:113]
	v_cvt_pk_bf16_f32 v192, v78, v79
	v_cvt_pk_bf16_f32 v193, v80, v81
	v_cvt_pk_bf16_f32 v182, v82, v83
	v_cvt_pk_bf16_f32 v183, v84, v85
	v_cvt_pk_bf16_f32 v184, v86, v87
	v_cvt_pk_bf16_f32 v185, v88, v89
	v_permlane32_swap_b32_e32 v224, v225
	s_waitcnt lgkmcnt(2)
	v_mfma_f32_32x32x16_bf16 v[114:129], v[244:247], v[134:137], v[114:129]
	v_permlane32_swap_b32_e32 v186, v188
	v_permlane32_swap_b32_e32 v187, v189
	v_permlane32_swap_b32_e32 v190, v192
	v_permlane32_swap_b32_e32 v191, v193
	s_waitcnt lgkmcnt(1)
	v_mfma_f32_32x32x16_bf16 v[98:113], v[178:181], v[130:133], v[98:113]
	v_cvt_pk_bf16_f32 v178, v90, v91
	v_cvt_pk_bf16_f32 v179, v92, v93
	v_cvt_pk_bf16_f32 v180, v94, v95
	v_cvt_pk_bf16_f32 v181, v96, v97
	v_permlane32_swap_b32_e32 v182, v184
	v_permlane32_swap_b32_e32 v183, v185
	s_waitcnt lgkmcnt(0)
	v_mfma_f32_32x32x16_bf16 v[114:129], v[248:251], v[130:133], v[114:129]
	v_permlane32_swap_b32_e32 v178, v180
	v_permlane32_swap_b32_e32 v179, v181
	v_cndmask_b32_e64 v214, 0, 1, s[40:41]
	v_cmp_ne_u32_e64 s[0:1], 1, v214
	s_andn2_b64 vcc, exec, s[40:41]
	s_cbranch_vccnz .Lfx_p3_tail
	s_waitcnt vmcnt(3)
	ds_write_b128 v206, v[162:165]
	s_waitcnt vmcnt(2)
	ds_write_b128 v206, v[166:169] offset:8192
	s_add_i32 s40, s38, 0x20000
	s_ashr_i32 s41, s40, 31
	s_lshl_b64 s[40:41], s[40:41], 1
	s_add_u32 s40, s36, s40
	s_addc_u32 s41, s37, s41
	v_lshl_add_u64 v[162:163], s[40:41], 0, v[194:195]
	v_add_co_u32_e32 v166, vcc, 0x20000, v162
	s_nop 1
	v_addc_co_u32_e32 v167, vcc, 0, v163, vcc
	global_load_dwordx4 v[162:165], v194, s[40:41]
	s_nop 0
	global_load_dwordx4 v[166:169], v[166:167], off
	s_branch .LBB0_1884
.Lfx_p3_tail:
	s_waitcnt vmcnt(1)
	ds_write_b128 v206, v[162:165]
	s_waitcnt vmcnt(0)
	ds_write_b128 v206, v[166:169] offset:8192

.LBB0_1886:
	ds_read_b64_tr_b16 v[226:227], v201 offset:0x4000
	ds_read_b64_tr_b16 v[228:229], v201 offset:0x4800
	ds_read_b64_tr_b16 v[230:231], v201 offset:0x5000
	ds_read_b64_tr_b16 v[232:233], v201 offset:0x5800
	ds_read_b64_tr_b16 v[234:235], v201 offset:0x6000
	ds_read_b64_tr_b16 v[236:237], v201 offset:0x6800
	ds_read_b64_tr_b16 v[238:239], v201 offset:0x7000
	ds_read_b64_tr_b16 v[240:241], v201 offset:0x7800
	s_waitcnt lgkmcnt(0)
	s_nop 0
	v_mfma_f32_32x32x16_bf16 v[50:65], v[186:189], v[226:229], v[50:65]
	v_max_f32_e32 v214, v99, v99
	v_max_f32_e32 v215, v98, v98
	v_max_f32_e32 v214, v215, v214
	v_max3_f32 v214, v214, v100, v101
	v_max3_f32 v214, v214, v102, v103
	v_max3_f32 v214, v214, v104, v105
	v_max3_f32 v214, v214, v106, v107
	v_mfma_f32_32x32x16_bf16 v[50:65], v[190:193], v[230:233], v[50:65]
	v_max3_f32 v214, v214, v108, v109
	v_max3_f32 v214, v214, v110, v111
	v_max3_f32 v214, v214, v112, v113
	ds_read_b64_tr_b16 v[242:243], v201 offset:0x4200
	v_max3_f32 v214, v214, v114, v115
	ds_read_b64_tr_b16 v[244:245], v201 offset:0x4a00
	v_max3_f32 v214, v214, v116, v117
	v_mfma_f32_32x32x16_bf16 v[50:65], v[182:185], v[234:237], v[50:65]
	ds_read_b64_tr_b16 v[246:247], v201 offset:0x5200
	v_max3_f32 v214, v214, v118, v119
	ds_read_b64_tr_b16 v[248:249], v201 offset:0x5a00
	v_max3_f32 v214, v214, v120, v121
	ds_read_b64_tr_b16 v[250:251], v201 offset:0x6200
	v_max3_f32 v214, v214, v122, v123
	ds_read_b64_tr_b16 v[252:253], v201 offset:0x6a00
	v_mfma_f32_32x32x16_bf16 v[50:65], v[178:181], v[238:241], v[50:65]
	v_max3_f32 v214, v214, v124, v125
	ds_read_b64_tr_b16 v[226:227], v201 offset:0x7200
	v_max3_f32 v214, v214, v126, v127
	ds_read_b64_tr_b16 v[228:229], v201 offset:0x7a00
	v_max3_f32 v214, v214, v128, v129
	v_mov_b32_e32 v215, v214
	s_waitcnt lgkmcnt(0)
	s_nop 1
	v_permlane32_swap_b32_e32 v214, v215
	v_max_f32_e32 v215, v215, v215
	v_max_f32_e32 v214, v214, v214
	v_max_f32_e32 v214, v214, v215
	v_mfma_f32_32x32x16_bf16 v[34:49], v[186:189], v[242:245], v[34:49]
	v_sub_f32_e32 v215, v214, v223
	ds_read_b64_tr_b16 v[230:231], v201 offset:0x4400
	v_mul_f32_e32 v215, 0x3db504f3, v215
	ds_read_b64_tr_b16 v[232:233], v201 offset:0x4c00
	v_cmp_ge_f32_e32 vcc, s51, v215
	ds_read_b64_tr_b16 v[234:235], v201 offset:0x5400
	s_cmp_eq_u64 vcc, exec
	v_mfma_f32_32x32x16_bf16 v[34:49], v[190:193], v[246:249], v[34:49]
	v_max_f32_e32 v215, v223, v223
	ds_read_b64_tr_b16 v[236:237], v201 offset:0x5c00
	v_max_f32_e32 v214, v215, v214
	s_cselect_b64 vcc, -1, 0
	ds_read_b64_tr_b16 v[238:239], v201 offset:0x6400
	v_cndmask_b32_e32 v215, v214, v223, vcc
	ds_read_b64_tr_b16 v[240:241], v201 offset:0x6c00
	v_mfma_f32_32x32x16_bf16 v[34:49], v[182:185], v[250:253], v[34:49]
	v_mul_f32_e32 v214, 0xbe0293ee, v215
	ds_read_b64_tr_b16 v[242:243], v201 offset:0x7400
	v_fma_f32 v112, v112, s14, v214
	v_fma_f32 v113, v113, s14, v214
	v_fma_f32 v110, v110, s14, v214
	v_fma_f32 v111, v111, s14, v214
	v_pk_fma_f32 v[108:109], v[108:109], s[14:15], v[214:215] op_sel_hi:[1,0,0]
	v_pk_fma_f32 v[106:107], v[106:107], s[14:15], v[214:215] op_sel_hi:[1,0,0]
	v_pk_fma_f32 v[104:105], v[104:105], s[14:15], v[214:215] op_sel_hi:[1,0,0]
	v_mfma_f32_32x32x16_bf16 v[34:49], v[178:181], v[226:229], v[34:49]
	v_fma_f32 v102, v102, s14, v214
	v_fma_f32 v103, v103, s14, v214
	v_fma_f32 v100, v100, s14, v214
	v_fma_f32 v101, v101, s14, v214
	v_fma_f32 v98, v98, s14, v214
	v_fma_f32 v99, v99, s14, v214
	v_pk_fma_f32 v[128:129], v[128:129], s[14:15], v[214:215] op_sel_hi:[1,0,0]
	v_pk_fma_f32 v[126:127], v[126:127], s[14:15], v[214:215] op_sel_hi:[1,0,0]
	v_pk_fma_f32 v[124:125], v[124:125], s[14:15], v[214:215] op_sel_hi:[1,0,0]
	v_pk_fma_f32 v[122:123], v[122:123], s[14:15], v[214:215] op_sel_hi:[1,0,0]
	v_pk_fma_f32 v[120:121], v[120:121], s[14:15], v[214:215] op_sel_hi:[1,0,0]
	v_pk_fma_f32 v[118:119], v[118:119], s[14:15], v[214:215] op_sel_hi:[1,0,0]
	v_pk_fma_f32 v[116:117], v[116:117], s[14:15], v[214:215] op_sel_hi:[1,0,0]
	v_pk_fma_f32 v[114:115], v[114:115], s[14:15], v[214:215] op_sel_hi:[1,0,0]
	ds_read_b64_tr_b16 v[244:245], v201 offset:0x7c00
	s_nop 0
	s_waitcnt lgkmcnt(0)
	v_mfma_f32_32x32x16_bf16 v[18:33], v[186:189], v[230:233], v[18:33]
	ds_read_b64_tr_b16 v[226:227], v201 offset:0x4600
	ds_read_b64_tr_b16 v[228:229], v201 offset:0x4e00
	ds_read_b64_tr_b16 v[230:231], v201 offset:0x5600
	ds_read_b64_tr_b16 v[232:233], v201 offset:0x5e00
	v_exp_f32_e32 v98, v98
	v_exp_f32_e32 v99, v99
	v_exp_f32_e32 v100, v100
	v_mfma_f32_32x32x16_bf16 v[18:33], v[190:193], v[234:237], v[18:33]
	ds_read_b64_tr_b16 v[234:235], v201 offset:0x6600
	ds_read_b64_tr_b16 v[236:237], v201 offset:0x6e00
	v_exp_f32_e32 v101, v101
	v_exp_f32_e32 v102, v102
	v_exp_f32_e32 v103, v103
	v_exp_f32_e32 v104, v104
	v_exp_f32_e32 v105, v105
	v_mfma_f32_32x32x16_bf16 v[18:33], v[182:185], v[238:241], v[18:33]
	ds_read_b64_tr_b16 v[238:239], v201 offset:0x7600
	ds_read_b64_tr_b16 v[240:241], v201 offset:0x7e00
	s_waitcnt lgkmcnt(0)
	v_mfma_f32_32x32x16_bf16 v[18:33], v[178:181], v[242:245], v[18:33]
	v_mfma_f32_32x32x16_bf16 v[2:17], v[186:189], v[226:229], v[2:17]
	v_exp_f32_e32 v106, v106
	v_exp_f32_e32 v107, v107
	v_exp_f32_e32 v108, v108
	v_exp_f32_e32 v109, v109
	v_exp_f32_e32 v110, v110
	v_exp_f32_e32 v111, v111
	v_exp_f32_e32 v112, v112
	v_mfma_f32_32x32x16_bf16 v[2:17], v[190:193], v[230:233], v[2:17]
	v_exp_f32_e32 v113, v113
	s_and_b64 vcc, exec, s[0:1]
	v_mfma_f32_32x32x16_bf16 v[2:17], v[182:185], v[234:237], v[2:17]
	v_mfma_f32_32x32x16_bf16 v[2:17], v[178:181], v[238:241], v[2:17]
	s_cbranch_vccnz .LBB0_1890
	s_waitcnt vmcnt(2)
	ds_write_b128 v208, v[170:173] offset:49152
	ds_write_b128 v208, v[174:177] offset:57344
	s_mov_b64 s[0:1], exec
	v_readlane_b32 s40, v254, 7
	v_readlane_b32 s41, v254, 8
	s_and_b64 s[40:41], s[0:1], s[40:41]
	s_mov_b64 exec, s[40:41]
	v_add_u32_e32 v179, 0, v198
	v_xor_b32_e32 v178, 0x80000000, v197
	v_add_u32_e32 v179, 0x11100, v179
	ds_write_b32 v179, v178
	s_or_b64 exec, exec, s[0:1]
